# static s_setprio 1 for waves 4-7 in the GEMM phases, per-segment priority flips in the K loops removed
# baseline (speedup 1.0000x reference)
.LBB0_194:
	s_add_i32 s55, s27, 0x18000
	s_mov_b64 s[20:21], 0x80
	s_bfe_u32 s6, s61, 0x20006
	v_lshl_add_u64 v[6:7], v[6:7], 0, s[20:21]
	s_mov_b32 m0, s55
	s_add_i32 s56, s27, 0x1a000
	s_lshl_b32 s7, s16, 13
	s_lshl_b32 s54, s6, 5
	s_lshl_b32 s22, s6, 12
	s_waitcnt vmcnt(2)
	s_barrier
	global_load_lds_dwordx4 v[6:7], off
	v_lshl_add_u64 v[4:5], v[4:5], 0, s[20:21]
	s_mov_b32 m0, s56
	s_add_i32 s57, s27, 0x8000
	s_add_i32 s58, s27, 0xa000
	global_load_lds_dwordx4 v[4:5], off
	v_lshl_add_u64 v[0:1], v[0:1], 0, s[20:21]
	s_mov_b32 m0, s57
	s_add_u32 s4, s44, 0x80080
	global_load_lds_dwordx4 v[0:1], off
	v_lshl_add_u64 v[0:1], v[2:3], 0, s[20:21]
	s_mov_b32 m0, s58
	s_addc_u32 s5, s45, 0
	s_add_i32 s59, s27, 0x1c000
	global_load_lds_dwordx4 v[0:1], off
	v_lshl_add_u64 v[0:1], s[4:5], 0, v[162:163]
	s_mov_b32 m0, s59
	s_add_i32 s60, s27, 0x1e000
	global_load_lds_dwordx4 v[0:1], off
	v_lshl_add_u64 v[0:1], s[4:5], 0, v[166:167]
	s_mov_b32 m0, s60
	v_and_b32_e32 v15, 15, v14
	global_load_lds_dwordx4 v[0:1], off
	s_waitcnt vmcnt(0)
	v_bfe_u32 v16, v14, 4, 2
	v_lshlrev_b32_e32 v14, 2, v14
	v_lshlrev_b32_e32 v17, 4, v16
	v_lshlrev_b32_e32 v18, 6, v15
	v_and_b32_e32 v14, 32, v14
	s_add_i32 s22, s22, 0
	v_bitop3_b32 v0, v18, v14, v17 bitop3:0x36
	s_cmpk_lt_u32 s61, 0x100
	v_lshl_or_b32 v171, s16, 6, v15
	v_add_u32_e32 v1, s22, v0
	s_cselect_b64 s[22:23], -1, 0
	s_lshl_b32 s16, s16, 11
	s_add_i32 s16, s16, 0
	v_lshlrev_b32_e32 v2, 5, v15
	s_add_i32 s26, s16, 0x20000
	v_add_u32_e32 v202, s26, v2
	s_add_i32 s26, s16, 0x20200
	v_add_u32_e32 v204, s26, v2
	s_add_i32 s26, s16, 0x20400
	v_add_u32_e32 v206, s26, v2
	s_add_i32 s26, s16, 0x20600
	v_add_u32_e32 v208, s26, v2
	s_add_i32 s26, s16, 0x21000
	v_add_u32_e32 v186, 0x10000, v1
	v_add_u32_e32 v187, 0x10400, v1
	v_add_u32_e32 v188, 0x10800, v1
	v_add_u32_e32 v189, 0x10c00, v1
	v_add_u32_e32 v190, 0x14000, v1
	v_add_u32_e32 v191, 0x14400, v1
	v_add_u32_e32 v192, 0x14800, v1
	v_add_u32_e32 v193, 0x14c00, v1
	v_add_u32_e32 v194, 0x18000, v1
	v_add_u32_e32 v195, 0x18400, v1
	v_add_u32_e32 v196, 0x18800, v1
	v_add_u32_e32 v197, 0x18c00, v1
	v_add_u32_e32 v198, 0x1c000, v1
	v_add_u32_e32 v199, 0x1c400, v1
	v_add_u32_e32 v200, 0x1c800, v1
	v_add_u32_e32 v201, 0x1cc00, v1
	v_add_u32_e32 v210, s26, v2
	s_add_i32 s26, s16, 0x21200
	v_lshlrev_b32_e32 v1, 15, v8
	v_add_u32_e32 v212, s26, v2
	s_add_i32 s26, s16, 0x21400
	s_add_i32 s16, s16, 0x21600
	v_and_b32_e32 v1, 0xffff0000, v1
	v_add_u32_e32 v214, s26, v2
	v_add_u32_e32 v216, s16, v2
	v_lshl_add_u32 v1, v9, 12, v1
	v_and_b32_e32 v2, 1, v8
	v_lshl_or_b32 v1, v2, 6, v1
	v_lshl_add_u32 v172, v10, 1, v1
	v_lshlrev_b32_e32 v1, 15, v11
	v_and_b32_e32 v1, 0xffff0000, v1
	s_waitcnt vmcnt(6)
	v_add_u32_e32 v0, 0, v0
	v_lshl_add_u32 v1, v12, 12, v1
	v_and_b32_e32 v2, 1, v11
	v_lshlrev_b32_e32 v170, 3, v16
	s_lshl_b32 s6, s6, 2
	v_lshl_or_b32 v1, v2, 6, v1
	v_add_u32_e32 v218, s7, v0
	v_mbcnt_lo_u32_b32 v0, -1, 0
	v_cmp_eq_u32_e64 s[4:5], 0, v16
	s_ashr_i32 s61, s46, 31
	s_ashr_i32 s63, s68, 31
	v_add_u32_e32 v203, s6, v202
	v_add_u32_e32 v205, s6, v204
	v_add_u32_e32 v207, s6, v206
	v_add_u32_e32 v209, s6, v208
	v_add_u32_e32 v211, s6, v210
	v_add_u32_e32 v213, s6, v212
	v_add_u32_e32 v215, s6, v214
	v_add_u32_e32 v217, s6, v216
	v_mov_b32_e32 v173, v169
	v_lshl_add_u32 v174, v13, 1, v1
	v_mov_b32_e32 v175, v169
	s_movk_i32 s64, 0x181
	s_mov_b32 s26, 0x3c800000
	v_mov_b32_e32 v219, 0x358637bd
	s_lshl_b32 s16, s54, 1
	v_lshlrev_b32_e32 v168, 1, v170
	v_mbcnt_hi_u32_b32 v220, -1, v0
	s_mov_b32 s65, s17
	s_barrier
	s_cmp_lt_u32 s94, 4
	s_cbranch_scc1 .Lsp200_skip
	s_setprio 1
.Lsp200_skip:
	s_branch .LBB0_197

.LBB0_200:
	s_add_u32 s72, s42, 0xfff80000
	s_addc_u32 s73, s43, -1
	s_mov_b32 m0, s57
	s_nop 0
	global_load_lds_dwordx4 v160, s[72:73]
	s_mov_b32 m0, s58
	s_nop 0
	global_load_lds_dwordx4 v164, s[72:73]
	ds_read_b128 v[16:19], v186
	ds_read_b128 v[20:23], v187
	ds_read_b128 v[24:27], v188
	ds_read_b128 v[28:31], v189
	ds_read_b128 v[0:3], v190
	ds_read_b128 v[4:7], v191
	ds_read_b128 v[8:11], v192
	ds_read_b128 v[12:15], v193
	s_add_u32 s44, s42, 0xfff80080
	s_addc_u32 s45, s43, -1
	s_cmp_eq_u32 s68, 28
	s_cselect_b32 s47, s31, s45
	s_cselect_b32 s46, s35, s44
	s_cselect_b32 s45, s29, s67
	s_cselect_b32 s44, s39, s66
	s_add_i32 m0, s27, 0xc000
	ds_read_b128 v[178:181], v218
	ds_read_b128 v[182:185], v218 offset:1024
	ds_read_b128 v[222:225], v218 offset:2048
	ds_read_b128 v[226:229], v218 offset:3072
	ds_read_b128 v[230:233], v218 offset:4096
	ds_read_b128 v[234:237], v218 offset:5120
	ds_read_b128 v[238:241], v218 offset:6144
	ds_read_b128 v[242:245], v218 offset:7168
	global_load_lds_dwordx4 v172, s[42:43]
	s_add_i32 m0, s27, 0xe000
	s_nop 0
	global_load_lds_dwordx4 v174, s[42:43]
	s_waitcnt vmcnt(8)
	s_waitcnt lgkmcnt(0)
	s_barrier
	s_waitcnt lgkmcnt(0)
	v_mfma_f32_16x16x128_f8f6f4 v[156:159], v[16:23], v[178:185], v[156:159]
	v_mfma_f32_16x16x128_f8f6f4 v[152:155], v[24:31], v[178:185], v[152:155]
	v_mfma_f32_16x16x128_f8f6f4 v[148:151], v[16:23], v[222:229], v[148:151]
	v_mfma_f32_16x16x128_f8f6f4 v[144:147], v[24:31], v[222:229], v[144:147]
	v_mfma_f32_16x16x128_f8f6f4 v[140:143], v[16:23], v[230:237], v[140:143]
	v_mfma_f32_16x16x128_f8f6f4 v[136:139], v[24:31], v[230:237], v[136:139]
	v_mfma_f32_16x16x128_f8f6f4 v[132:135], v[16:23], v[238:245], v[132:135]
	v_mfma_f32_16x16x128_f8f6f4 v[128:131], v[24:31], v[238:245], v[128:131]
	v_mfma_f32_16x16x128_f8f6f4 v[124:127], v[0:7], v[178:185], v[124:127]
	v_mfma_f32_16x16x128_f8f6f4 v[120:123], v[8:15], v[178:185], v[120:123]
	v_mfma_f32_16x16x128_f8f6f4 v[116:119], v[0:7], v[222:229], v[116:119]
	v_mfma_f32_16x16x128_f8f6f4 v[112:115], v[8:15], v[222:229], v[112:115]
	v_mfma_f32_16x16x128_f8f6f4 v[108:111], v[0:7], v[230:237], v[108:111]
	v_mfma_f32_16x16x128_f8f6f4 v[104:107], v[8:15], v[230:237], v[104:107]
	v_mfma_f32_16x16x128_f8f6f4 v[100:103], v[0:7], v[238:245], v[100:103]
	v_mfma_f32_16x16x128_f8f6f4 v[96:99], v[8:15], v[238:245], v[96:99]
	s_barrier
	s_mov_b32 m0, s33
	v_lshl_add_u64 v[178:179], s[44:45], 0, v[162:163]
	s_add_u32 s70, s44, 0x80000
	ds_read_b128 v[222:225], v218 offset:16384
	ds_read_b128 v[226:229], v218 offset:17408
	ds_read_b128 v[230:233], v218 offset:18432
	ds_read_b128 v[234:237], v218 offset:19456
	ds_read_b128 v[238:241], v218 offset:20480
	ds_read_b128 v[242:245], v218 offset:21504
	ds_read_b128 v[246:249], v218 offset:22528
	ds_read_b128 v[250:253], v218 offset:23552
	global_load_lds_dwordx4 v[178:179], off
	v_lshl_add_u64 v[180:181], s[44:45], 0, v[166:167]
	s_mov_b32 m0, s48
	s_addc_u32 s71, s45, 0
	global_load_lds_dwordx4 v[180:181], off
	s_mov_b32 m0, s49
	s_nop 0
	global_load_lds_dwordx4 v162, s[70:71]
	s_mov_b32 m0, s50
	s_nop 0
	global_load_lds_dwordx4 v166, s[70:71]
	s_waitcnt vmcnt(6)
	s_waitcnt lgkmcnt(0)
	s_barrier
	s_waitcnt lgkmcnt(0)
	v_mfma_f32_16x16x128_f8f6f4 v[92:95], v[16:23], v[222:229], v[92:95]
	v_mfma_f32_16x16x128_f8f6f4 v[88:91], v[24:31], v[222:229], v[88:91]
	v_mfma_f32_16x16x128_f8f6f4 v[84:87], v[16:23], v[230:237], v[84:87]
	v_mfma_f32_16x16x128_f8f6f4 v[80:83], v[24:31], v[230:237], v[80:83]
	v_mfma_f32_16x16x128_f8f6f4 v[76:79], v[16:23], v[238:245], v[76:79]
	v_mfma_f32_16x16x128_f8f6f4 v[72:75], v[24:31], v[238:245], v[72:75]
	v_mfma_f32_16x16x128_f8f6f4 v[68:71], v[16:23], v[246:253], v[68:71]
	v_mfma_f32_16x16x128_f8f6f4 v[64:67], v[24:31], v[246:253], v[64:67]
	v_mfma_f32_16x16x128_f8f6f4 v[60:63], v[0:7], v[222:229], v[60:63]
	v_mfma_f32_16x16x128_f8f6f4 v[56:59], v[8:15], v[222:229], v[56:59]
	v_mfma_f32_16x16x128_f8f6f4 v[52:55], v[0:7], v[230:237], v[52:55]
	v_mfma_f32_16x16x128_f8f6f4 v[48:51], v[8:15], v[230:237], v[48:51]
	v_mfma_f32_16x16x128_f8f6f4 v[44:47], v[0:7], v[238:245], v[44:47]
	v_mfma_f32_16x16x128_f8f6f4 v[40:43], v[8:15], v[238:245], v[40:43]
	v_mfma_f32_16x16x128_f8f6f4 v[36:39], v[0:7], v[246:253], v[36:39]
	v_mfma_f32_16x16x128_f8f6f4 v[32:35], v[8:15], v[246:253], v[32:35]
	s_barrier
	s_mov_b32 m0, s27
	s_nop 0
	global_load_lds_dwordx4 v160, s[46:47]
	s_mov_b32 m0, s51
	s_nop 0
	global_load_lds_dwordx4 v164, s[46:47]
	ds_read_b128 v[0:3], v194
	ds_read_b128 v[4:7], v195
	ds_read_b128 v[8:11], v196
	ds_read_b128 v[12:15], v197
	ds_read_b128 v[16:19], v198
	ds_read_b128 v[20:23], v199
	ds_read_b128 v[24:27], v200
	ds_read_b128 v[28:31], v201
	s_add_u32 s46, s46, 0x80000
	s_addc_u32 s47, s47, 0
	s_mov_b32 m0, s52
	ds_read_b128 v[222:225], v218 offset:32768
	ds_read_b128 v[226:229], v218 offset:33792
	ds_read_b128 v[230:233], v218 offset:34816
	ds_read_b128 v[234:237], v218 offset:35840
	ds_read_b128 v[238:241], v218 offset:36864
	ds_read_b128 v[242:245], v218 offset:37888
	ds_read_b128 v[246:249], v218 offset:38912
	ds_read_b128 v[250:253], v218 offset:39936
	global_load_lds_dwordx4 v160, s[46:47]
	s_mov_b32 m0, s53
	s_nop 0
	global_load_lds_dwordx4 v164, s[46:47]
	s_waitcnt vmcnt(8)
	s_waitcnt lgkmcnt(0)
	s_barrier
	s_waitcnt lgkmcnt(0)
	v_mfma_f32_16x16x128_f8f6f4 v[156:159], v[0:7], v[222:229], v[156:159]
	v_mfma_f32_16x16x128_f8f6f4 v[152:155], v[8:15], v[222:229], v[152:155]
	v_mfma_f32_16x16x128_f8f6f4 v[148:151], v[0:7], v[230:237], v[148:151]
	v_mfma_f32_16x16x128_f8f6f4 v[144:147], v[8:15], v[230:237], v[144:147]
	v_mfma_f32_16x16x128_f8f6f4 v[140:143], v[0:7], v[238:245], v[140:143]
	v_mfma_f32_16x16x128_f8f6f4 v[136:139], v[8:15], v[238:245], v[136:139]
	v_mfma_f32_16x16x128_f8f6f4 v[132:135], v[0:7], v[246:253], v[132:135]
	v_mfma_f32_16x16x128_f8f6f4 v[128:131], v[8:15], v[246:253], v[128:131]
	v_mfma_f32_16x16x128_f8f6f4 v[124:127], v[16:23], v[222:229], v[124:127]
	v_mfma_f32_16x16x128_f8f6f4 v[120:123], v[24:31], v[222:229], v[120:123]
	v_mfma_f32_16x16x128_f8f6f4 v[116:119], v[16:23], v[230:237], v[116:119]
	v_mfma_f32_16x16x128_f8f6f4 v[112:115], v[24:31], v[230:237], v[112:115]
	v_mfma_f32_16x16x128_f8f6f4 v[108:111], v[16:23], v[238:245], v[108:111]
	v_mfma_f32_16x16x128_f8f6f4 v[104:107], v[24:31], v[238:245], v[104:107]
	v_mfma_f32_16x16x128_f8f6f4 v[100:103], v[16:23], v[246:253], v[100:103]
	v_mfma_f32_16x16x128_f8f6f4 v[96:99], v[24:31], v[246:253], v[96:99]
	s_barrier
	s_mov_b32 m0, s55
	v_lshl_add_u64 v[176:177], v[178:179], 0, s[20:21]
	s_add_u32 s44, s44, 0x80080
	ds_read_b128 v[222:225], v218 offset:49152
	ds_read_b128 v[226:229], v218 offset:50176
	ds_read_b128 v[230:233], v218 offset:51200
	ds_read_b128 v[234:237], v218 offset:52224
	ds_read_b128 v[238:241], v218 offset:53248
	ds_read_b128 v[242:245], v218 offset:54272
	ds_read_b128 v[246:249], v218 offset:55296
	ds_read_b128 v[250:253], v218 offset:56320
	global_load_lds_dwordx4 v[176:177], off
	v_lshl_add_u64 v[176:177], v[180:181], 0, s[20:21]
	s_mov_b32 m0, s56
	s_addc_u32 s45, s45, 0
	global_load_lds_dwordx4 v[176:177], off
	s_mov_b32 m0, s59
	s_nop 0
	global_load_lds_dwordx4 v162, s[44:45]
	s_mov_b32 m0, s60
	s_nop 0
	global_load_lds_dwordx4 v166, s[44:45]
	s_waitcnt vmcnt(6)
	s_waitcnt lgkmcnt(0)
	s_barrier
	s_waitcnt lgkmcnt(0)
	v_mfma_f32_16x16x128_f8f6f4 v[92:95], v[0:7], v[222:229], v[92:95]
	v_mfma_f32_16x16x128_f8f6f4 v[88:91], v[8:15], v[222:229], v[88:91]
	v_mfma_f32_16x16x128_f8f6f4 v[84:87], v[0:7], v[230:237], v[84:87]
	v_mfma_f32_16x16x128_f8f6f4 v[80:83], v[8:15], v[230:237], v[80:83]
	v_mfma_f32_16x16x128_f8f6f4 v[76:79], v[0:7], v[238:245], v[76:79]
	v_mfma_f32_16x16x128_f8f6f4 v[72:75], v[8:15], v[238:245], v[72:75]
	v_mfma_f32_16x16x128_f8f6f4 v[68:71], v[0:7], v[246:253], v[68:71]
	v_mfma_f32_16x16x128_f8f6f4 v[64:67], v[8:15], v[246:253], v[64:67]
	v_mfma_f32_16x16x128_f8f6f4 v[60:63], v[16:23], v[222:229], v[60:63]
	v_mfma_f32_16x16x128_f8f6f4 v[56:59], v[24:31], v[222:229], v[56:59]
	v_mfma_f32_16x16x128_f8f6f4 v[52:55], v[16:23], v[230:237], v[52:55]
	v_mfma_f32_16x16x128_f8f6f4 v[48:51], v[24:31], v[230:237], v[48:51]
	v_mfma_f32_16x16x128_f8f6f4 v[44:47], v[16:23], v[238:245], v[44:47]
	v_mfma_f32_16x16x128_f8f6f4 v[40:43], v[24:31], v[238:245], v[40:43]
	v_mfma_f32_16x16x128_f8f6f4 v[36:39], v[16:23], v[246:253], v[36:39]
	v_mfma_f32_16x16x128_f8f6f4 v[32:35], v[24:31], v[246:253], v[32:35]
	s_barrier
	s_add_i32 s68, s68, 2
	s_add_u32 s42, s42, 0x100
	s_addc_u32 s43, s43, 0
	s_add_u32 s66, s66, 0x100
	s_addc_u32 s67, s67, 0
	s_cmp_gt_u32 s68, 29
	s_cbranch_scc0 .LBB0_200
	s_nop 15
	s_nop 15
	s_and_b64 vcc, exec, s[22:23]
	s_cbranch_vccz .LBB0_203
	s_barrier

.LBB0_251:
	s_setprio 0
	s_waitcnt vmcnt(0)
	v_readlane_b32 s46, v254, 18
	v_readlane_b32 s61, v254, 20
	s_barrier
	v_readlane_b32 s47, v254, 19

.LBB0_552:
	v_readlane_b32 s4, v254, 0
	v_readlane_b32 s5, v254, 1
	s_load_dwordx2 s[4:5], s[4:5], 0xa0
	s_mov_b64 s[14:15], 0x80
	v_lshl_add_u64 v[6:7], v[6:7], 0, s[14:15]
	s_waitcnt vmcnt(2)
	s_barrier
	s_waitcnt lgkmcnt(0)
	s_add_u32 s12, s4, 0x4d400000
	s_addc_u32 s13, s5, 0
	s_add_u32 s45, s4, 0x18000
	s_addc_u32 s46, s5, 0
	s_lshl_b32 s4, s94, 5
	s_add_i32 s47, s29, 0x18000
	s_and_b32 s20, s4, 0x60
	s_mov_b32 m0, s47
	s_add_i32 s48, s29, 0x1a000
	s_lshl_b32 s18, s17, 13
	s_lshl_b32 s21, s20, 7
	global_load_lds_dwordx4 v[6:7], off
	v_lshl_add_u64 v[4:5], v[4:5], 0, s[14:15]
	s_mov_b32 m0, s48
	s_add_i32 s49, s29, 0x8000
	s_add_i32 s50, s29, 0xa000
	global_load_lds_dwordx4 v[4:5], off
	v_lshl_add_u64 v[0:1], v[0:1], 0, s[14:15]
	s_mov_b32 m0, s49
	s_add_u32 s4, s34, 0x80080
	global_load_lds_dwordx4 v[0:1], off
	v_lshl_add_u64 v[0:1], v[2:3], 0, s[14:15]
	s_mov_b32 m0, s50
	s_addc_u32 s5, s35, 0
	s_add_i32 s51, s29, 0x1c000
	global_load_lds_dwordx4 v[0:1], off
	v_lshl_add_u64 v[0:1], s[4:5], 0, v[160:161]
	s_mov_b32 m0, s51
	s_add_i32 s52, s29, 0x1e000
	global_load_lds_dwordx4 v[0:1], off
	v_lshl_add_u64 v[0:1], s[4:5], 0, v[162:163]
	s_mov_b32 m0, s52
	v_lshlrev_b32_e32 v3, 2, v12
	global_load_lds_dwordx4 v[0:1], off
	v_and_b32_e32 v0, 15, v12
	v_bfe_u32 v1, v12, 4, 2
	v_lshl_or_b32 v180, s17, 6, v0
	v_lshlrev_b32_e32 v2, 4, v1
	v_lshlrev_b32_e32 v0, 6, v0
	v_and_b32_e32 v3, 32, v3
	v_bitop3_b32 v0, v0, v3, v2 bitop3:0x36
	s_add_i32 s21, s21, 0
	v_lshl_or_b32 v197, v1, 2, s20
	v_lshlrev_b32_e32 v1, 15, v8
	v_add_u32_e32 v2, s21, v0
	v_and_b32_e32 v1, 0xffff0000, v1
	v_add_u32_e32 v181, 0x10000, v2
	v_add_u32_e32 v182, 0x10400, v2
	v_add_u32_e32 v183, 0x10800, v2
	v_add_u32_e32 v184, 0x10c00, v2
	v_add_u32_e32 v185, 0x14000, v2
	v_add_u32_e32 v186, 0x14400, v2
	v_add_u32_e32 v187, 0x14800, v2
	v_add_u32_e32 v188, 0x14c00, v2
	v_add_u32_e32 v189, 0x18000, v2
	v_add_u32_e32 v190, 0x18400, v2
	v_add_u32_e32 v191, 0x18800, v2
	v_add_u32_e32 v192, 0x18c00, v2
	v_add_u32_e32 v193, 0x1c000, v2
	v_add_u32_e32 v194, 0x1c400, v2
	v_add_u32_e32 v195, 0x1c800, v2
	v_add_u32_e32 v196, 0x1cc00, v2
	v_lshl_add_u32 v1, v9, 12, v1
	v_and_b32_e32 v2, 1, v8
	v_lshl_or_b32 v1, v2, 6, v1
	v_lshl_add_u32 v164, v10, 1, v1
	v_lshlrev_b32_e32 v1, 15, v11
	v_and_b32_e32 v1, 0xffff0000, v1
	s_waitcnt vmcnt(6)
	v_lshl_add_u32 v1, v13, 12, v1
	v_and_b32_e32 v2, 1, v11
	v_add_u32_e32 v0, 0, v0
	s_cmpk_lt_u32 s65, 0x100
	v_lshl_or_b32 v1, v2, 6, v1
	s_sext_i32_i8 s54, s16
	s_cselect_b64 s[16:17], -1, 0
	s_ashr_i32 s53, s64, 31
	v_mov_b32_e32 v165, v161
	v_lshl_add_u32 v166, v14, 1, v1
	v_mov_b32_e32 v167, v161
	v_mov_b64_e32 v[168:169], 0x400
	v_mov_b64_e32 v[170:171], 0x3ff
	v_add_u32_e32 v198, s18, v0
	s_mov_b32 s18, 0x3a800000
	s_barrier
	s_cmp_lt_u32 s94, 4
	s_cbranch_scc1 .Lsp562_skip
	s_setprio 1

.LBB0_562:
	s_add_u32 s72, s30, 0xfff80000
	s_addc_u32 s73, s31, -1
	s_mov_b32 m0, s49
	s_nop 0
	global_load_lds_dwordx4 v160, s[72:73]
	s_mov_b32 m0, s50
	s_nop 0
	global_load_lds_dwordx4 v162, s[72:73]
	ds_read_b128 v[16:19], v181
	ds_read_b128 v[20:23], v182
	ds_read_b128 v[24:27], v183
	ds_read_b128 v[28:31], v184
	ds_read_b128 v[0:3], v185
	ds_read_b128 v[4:7], v186
	ds_read_b128 v[8:11], v187
	ds_read_b128 v[12:15], v188
	s_add_u32 s34, s30, 0xfff80080
	s_addc_u32 s35, s31, -1
	s_cmp_eq_u32 s59, 28
	s_cselect_b32 s37, s23, s35
	s_cselect_b32 s36, s55, s34
	s_cselect_b32 s35, s21, s58
	s_cselect_b32 s34, s56, s57
	s_add_i32 m0, s29, 0xc000
	ds_read_b128 v[172:175], v198
	ds_read_b128 v[176:179], v198 offset:1024
	ds_read_b128 v[200:203], v198 offset:2048
	ds_read_b128 v[204:207], v198 offset:3072
	ds_read_b128 v[208:211], v198 offset:4096
	ds_read_b128 v[212:215], v198 offset:5120
	ds_read_b128 v[216:219], v198 offset:6144
	ds_read_b128 v[220:223], v198 offset:7168
	global_load_lds_dwordx4 v164, s[30:31]
	s_add_i32 m0, s29, 0xe000
	s_nop 0
	global_load_lds_dwordx4 v166, s[30:31]
	s_waitcnt vmcnt(8)
	s_waitcnt lgkmcnt(0)
	s_barrier
	s_waitcnt lgkmcnt(0)
	v_mfma_f32_16x16x128_f8f6f4 v[156:159], v[16:23], v[172:179], v[156:159]
	v_mfma_f32_16x16x128_f8f6f4 v[152:155], v[24:31], v[172:179], v[152:155]
	v_mfma_f32_16x16x128_f8f6f4 v[148:151], v[16:23], v[200:207], v[148:151]
	v_mfma_f32_16x16x128_f8f6f4 v[144:147], v[24:31], v[200:207], v[144:147]
	v_mfma_f32_16x16x128_f8f6f4 v[124:127], v[16:23], v[208:215], v[124:127]
	v_mfma_f32_16x16x128_f8f6f4 v[120:123], v[24:31], v[208:215], v[120:123]
	v_mfma_f32_16x16x128_f8f6f4 v[116:119], v[16:23], v[216:223], v[116:119]
	v_mfma_f32_16x16x128_f8f6f4 v[112:115], v[24:31], v[216:223], v[112:115]
	v_mfma_f32_16x16x128_f8f6f4 v[140:143], v[0:7], v[172:179], v[140:143]
	v_mfma_f32_16x16x128_f8f6f4 v[136:139], v[8:15], v[172:179], v[136:139]
	v_mfma_f32_16x16x128_f8f6f4 v[132:135], v[0:7], v[200:207], v[132:135]
	v_mfma_f32_16x16x128_f8f6f4 v[128:131], v[8:15], v[200:207], v[128:131]
	v_mfma_f32_16x16x128_f8f6f4 v[108:111], v[0:7], v[208:215], v[108:111]
	v_mfma_f32_16x16x128_f8f6f4 v[104:107], v[8:15], v[208:215], v[104:107]
	v_mfma_f32_16x16x128_f8f6f4 v[100:103], v[0:7], v[216:223], v[100:103]
	v_mfma_f32_16x16x128_f8f6f4 v[96:99], v[8:15], v[216:223], v[96:99]
	s_barrier
	s_mov_b32 m0, s33
	v_lshl_add_u64 v[172:173], s[34:35], 0, v[160:161]
	s_add_u32 s60, s34, 0x80000
	ds_read_b128 v[200:203], v198 offset:16384
	ds_read_b128 v[204:207], v198 offset:17408
	ds_read_b128 v[208:211], v198 offset:18432
	ds_read_b128 v[212:215], v198 offset:19456
	ds_read_b128 v[216:219], v198 offset:20480
	ds_read_b128 v[220:223], v198 offset:21504
	ds_read_b128 v[224:227], v198 offset:22528
	ds_read_b128 v[228:231], v198 offset:23552
	global_load_lds_dwordx4 v[172:173], off
	v_lshl_add_u64 v[174:175], s[34:35], 0, v[162:163]
	s_mov_b32 m0, s38
	s_addc_u32 s61, s35, 0
	global_load_lds_dwordx4 v[174:175], off
	s_mov_b32 m0, s39
	s_nop 0
	global_load_lds_dwordx4 v160, s[60:61]
	s_mov_b32 m0, s40
	s_nop 0
	global_load_lds_dwordx4 v162, s[60:61]
	s_waitcnt vmcnt(6)
	s_waitcnt lgkmcnt(0)
	s_barrier
	s_waitcnt lgkmcnt(0)
	v_mfma_f32_16x16x128_f8f6f4 v[92:95], v[16:23], v[200:207], v[92:95]
	v_mfma_f32_16x16x128_f8f6f4 v[88:91], v[24:31], v[200:207], v[88:91]
	v_mfma_f32_16x16x128_f8f6f4 v[84:87], v[16:23], v[208:215], v[84:87]
	v_mfma_f32_16x16x128_f8f6f4 v[80:83], v[24:31], v[208:215], v[80:83]
	v_mfma_f32_16x16x128_f8f6f4 v[60:63], v[16:23], v[216:223], v[60:63]
	v_mfma_f32_16x16x128_f8f6f4 v[56:59], v[24:31], v[216:223], v[56:59]
	v_mfma_f32_16x16x128_f8f6f4 v[52:55], v[16:23], v[224:231], v[52:55]
	v_mfma_f32_16x16x128_f8f6f4 v[48:51], v[24:31], v[224:231], v[48:51]
	v_mfma_f32_16x16x128_f8f6f4 v[76:79], v[0:7], v[200:207], v[76:79]
	v_mfma_f32_16x16x128_f8f6f4 v[72:75], v[8:15], v[200:207], v[72:75]
	v_mfma_f32_16x16x128_f8f6f4 v[68:71], v[0:7], v[208:215], v[68:71]
	v_mfma_f32_16x16x128_f8f6f4 v[64:67], v[8:15], v[208:215], v[64:67]
	v_mfma_f32_16x16x128_f8f6f4 v[44:47], v[0:7], v[216:223], v[44:47]
	v_mfma_f32_16x16x128_f8f6f4 v[40:43], v[8:15], v[216:223], v[40:43]
	v_mfma_f32_16x16x128_f8f6f4 v[36:39], v[0:7], v[224:231], v[36:39]
	v_mfma_f32_16x16x128_f8f6f4 v[32:35], v[8:15], v[224:231], v[32:35]
	s_barrier
	s_mov_b32 m0, s29
	s_nop 0
	global_load_lds_dwordx4 v160, s[36:37]
	s_mov_b32 m0, s41
	s_nop 0
	global_load_lds_dwordx4 v162, s[36:37]
	ds_read_b128 v[0:3], v189
	ds_read_b128 v[4:7], v190
	ds_read_b128 v[8:11], v191
	ds_read_b128 v[12:15], v192
	ds_read_b128 v[16:19], v193
	ds_read_b128 v[20:23], v194
	ds_read_b128 v[24:27], v195
	ds_read_b128 v[28:31], v196
	s_add_u32 s36, s36, 0x80000
	s_addc_u32 s37, s37, 0
	s_mov_b32 m0, s42
	ds_read_b128 v[200:203], v198 offset:32768
	ds_read_b128 v[204:207], v198 offset:33792
	ds_read_b128 v[208:211], v198 offset:34816
	ds_read_b128 v[212:215], v198 offset:35840
	ds_read_b128 v[216:219], v198 offset:36864
	ds_read_b128 v[220:223], v198 offset:37888
	ds_read_b128 v[224:227], v198 offset:38912
	ds_read_b128 v[228:231], v198 offset:39936
	global_load_lds_dwordx4 v160, s[36:37]
	s_mov_b32 m0, s43
	s_nop 0
	global_load_lds_dwordx4 v162, s[36:37]
	s_waitcnt vmcnt(8)
	s_waitcnt lgkmcnt(0)
	s_barrier
	s_waitcnt lgkmcnt(0)
	v_mfma_f32_16x16x128_f8f6f4 v[156:159], v[0:7], v[200:207], v[156:159]
	v_mfma_f32_16x16x128_f8f6f4 v[152:155], v[8:15], v[200:207], v[152:155]
	v_mfma_f32_16x16x128_f8f6f4 v[148:151], v[0:7], v[208:215], v[148:151]
	v_mfma_f32_16x16x128_f8f6f4 v[144:147], v[8:15], v[208:215], v[144:147]
	v_mfma_f32_16x16x128_f8f6f4 v[124:127], v[0:7], v[216:223], v[124:127]
	v_mfma_f32_16x16x128_f8f6f4 v[120:123], v[8:15], v[216:223], v[120:123]
	v_mfma_f32_16x16x128_f8f6f4 v[116:119], v[0:7], v[224:231], v[116:119]
	v_mfma_f32_16x16x128_f8f6f4 v[112:115], v[8:15], v[224:231], v[112:115]
	v_mfma_f32_16x16x128_f8f6f4 v[140:143], v[16:23], v[200:207], v[140:143]
	v_mfma_f32_16x16x128_f8f6f4 v[136:139], v[24:31], v[200:207], v[136:139]
	v_mfma_f32_16x16x128_f8f6f4 v[132:135], v[16:23], v[208:215], v[132:135]
	v_mfma_f32_16x16x128_f8f6f4 v[128:131], v[24:31], v[208:215], v[128:131]
	v_mfma_f32_16x16x128_f8f6f4 v[108:111], v[16:23], v[216:223], v[108:111]
	v_mfma_f32_16x16x128_f8f6f4 v[104:107], v[24:31], v[216:223], v[104:107]
	v_mfma_f32_16x16x128_f8f6f4 v[100:103], v[16:23], v[224:231], v[100:103]
	v_mfma_f32_16x16x128_f8f6f4 v[96:99], v[24:31], v[224:231], v[96:99]
	s_barrier
	s_mov_b32 m0, s47
	v_lshl_add_u64 v[172:173], v[172:173], 0, s[14:15]
	s_add_u32 s34, s34, 0x80080
	ds_read_b128 v[200:203], v198 offset:49152
	ds_read_b128 v[204:207], v198 offset:50176
	ds_read_b128 v[208:211], v198 offset:51200
	ds_read_b128 v[212:215], v198 offset:52224
	ds_read_b128 v[216:219], v198 offset:53248
	ds_read_b128 v[220:223], v198 offset:54272
	ds_read_b128 v[224:227], v198 offset:55296
	ds_read_b128 v[228:231], v198 offset:56320
	global_load_lds_dwordx4 v[172:173], off
	v_lshl_add_u64 v[172:173], v[174:175], 0, s[14:15]
	s_mov_b32 m0, s48
	s_addc_u32 s35, s35, 0
	global_load_lds_dwordx4 v[172:173], off
	s_mov_b32 m0, s51
	s_nop 0
	global_load_lds_dwordx4 v160, s[34:35]
	s_mov_b32 m0, s52
	s_nop 0
	global_load_lds_dwordx4 v162, s[34:35]
	s_waitcnt vmcnt(6)
	s_waitcnt lgkmcnt(0)
	s_barrier
	s_waitcnt lgkmcnt(0)
	v_mfma_f32_16x16x128_f8f6f4 v[92:95], v[0:7], v[200:207], v[92:95]
	v_mfma_f32_16x16x128_f8f6f4 v[88:91], v[8:15], v[200:207], v[88:91]
	v_mfma_f32_16x16x128_f8f6f4 v[84:87], v[0:7], v[208:215], v[84:87]
	v_mfma_f32_16x16x128_f8f6f4 v[80:83], v[8:15], v[208:215], v[80:83]
	v_mfma_f32_16x16x128_f8f6f4 v[60:63], v[0:7], v[216:223], v[60:63]
	v_mfma_f32_16x16x128_f8f6f4 v[56:59], v[8:15], v[216:223], v[56:59]
	v_mfma_f32_16x16x128_f8f6f4 v[52:55], v[0:7], v[224:231], v[52:55]
	v_mfma_f32_16x16x128_f8f6f4 v[48:51], v[8:15], v[224:231], v[48:51]
	v_mfma_f32_16x16x128_f8f6f4 v[76:79], v[16:23], v[200:207], v[76:79]
	v_mfma_f32_16x16x128_f8f6f4 v[72:75], v[24:31], v[200:207], v[72:75]
	v_mfma_f32_16x16x128_f8f6f4 v[68:71], v[16:23], v[208:215], v[68:71]
	v_mfma_f32_16x16x128_f8f6f4 v[64:67], v[24:31], v[208:215], v[64:67]
	v_mfma_f32_16x16x128_f8f6f4 v[44:47], v[16:23], v[216:223], v[44:47]
	v_mfma_f32_16x16x128_f8f6f4 v[40:43], v[24:31], v[216:223], v[40:43]
	v_mfma_f32_16x16x128_f8f6f4 v[36:39], v[16:23], v[224:231], v[36:39]
	v_mfma_f32_16x16x128_f8f6f4 v[32:35], v[24:31], v[224:231], v[32:35]
	s_barrier
	s_add_i32 s59, s59, 2
	s_add_u32 s30, s30, 0x100
	s_addc_u32 s31, s31, 0
	s_add_u32 s57, s57, 0x100
	s_addc_u32 s58, s58, 0
	s_cmp_gt_u32 s59, 29
	s_cbranch_scc0 .LBB0_562
	s_nop 15
	s_nop 15
	s_and_b64 vcc, exec, s[16:17]
	s_cbranch_vccz .LBB0_565
	s_barrier

.LBB0_568:
	s_setprio 0
	s_waitcnt vmcnt(0)
	s_barrier

.LBB0_677:
	s_add_i32 s42, s33, 0x18000
	s_mov_b64 s[10:11], 0x80
	v_lshl_add_u64 v[6:7], v[6:7], 0, s[10:11]
	s_mov_b32 m0, s42
	s_add_i32 s43, s33, 0x1a000
	s_bfe_u32 s5, s65, 0x20006
	s_lshl_b32 s16, s31, 13
	s_waitcnt vmcnt(2)
	s_barrier
	global_load_lds_dwordx4 v[6:7], off
	v_lshl_add_u64 v[4:5], v[4:5], 0, s[10:11]
	s_mov_b32 m0, s43
	s_add_i32 s44, s33, 0x8000
	s_add_i32 s45, s33, 0xa000
	global_load_lds_dwordx4 v[4:5], off
	v_lshl_add_u64 v[0:1], v[0:1], 0, s[10:11]
	s_mov_b32 m0, s44
	s_add_u32 s12, s26, 0x100080
	global_load_lds_dwordx4 v[0:1], off
	v_lshl_add_u64 v[0:1], v[2:3], 0, s[10:11]
	s_mov_b32 m0, s45
	s_addc_u32 s13, s27, 0
	s_add_i32 s46, s33, 0x1c000
	global_load_lds_dwordx4 v[0:1], off
	v_lshl_add_u64 v[0:1], s[12:13], 0, v[128:129]
	s_mov_b32 m0, s46
	s_add_i32 s47, s33, 0x1e000
	global_load_lds_dwordx4 v[0:1], off
	v_lshl_add_u64 v[0:1], s[12:13], 0, v[130:131]
	s_mov_b32 m0, s47
	s_cmpk_lt_u32 s65, 0x100
	global_load_lds_dwordx4 v[0:1], off
	v_and_b32_e32 v0, 15, v14
	v_bfe_u32 v1, v14, 4, 2
	v_lshlrev_b32_e32 v2, 6, v0
	v_lshlrev_b32_e32 v0, 2, v0
	v_lshl_or_b32 v2, v1, 4, v2
	v_and_b32_e32 v3, 32, v0
	s_sext_i32_i8 s15, s4
	v_xad_u32 v4, v2, v3, 0
	s_cselect_b64 s[12:13], -1, 0
	s_lshl_b32 s4, s5, 13
	v_lshl_add_u32 v5, s5, 12, v4
	v_lshl_or_b32 v2, v1, 10, s4
	v_readlane_b32 s4, v254, 0
	v_readlane_b32 s5, v254, 1
	s_load_dwordx2 s[4:5], s[4:5], 0xa0
	v_mov_b32_e32 v1, v129
	v_mov_b32_e32 v3, v129
	s_waitcnt vmcnt(6)
	v_add_u32_e32 v142, 0x10000, v5
	s_waitcnt lgkmcnt(0)
	v_lshl_add_u64 v[0:1], s[4:5], 0, v[0:1]
	v_lshl_add_u64 v[0:1], v[0:1], 0, v[2:3]
	s_mov_b64 s[4:5], 0x41400000
	v_lshl_add_u64 v[132:133], v[0:1], 0, s[4:5]
	v_lshlrev_b32_e32 v0, 16, v8
	v_and_b32_e32 v0, 0xfffe0000, v0
	v_lshl_add_u32 v0, v9, 13, v0
	v_and_b32_e32 v1, 1, v8
	v_lshl_or_b32 v0, v1, 6, v0
	v_lshl_add_u32 v134, v10, 1, v0
	v_lshlrev_b32_e32 v0, 16, v11
	v_and_b32_e32 v0, 0xfffe0000, v0
	v_lshl_add_u32 v0, v12, 13, v0
	v_and_b32_e32 v1, 1, v11
	v_lshl_or_b32 v0, v1, 6, v0
	v_add_u32_e32 v143, 0x10400, v5
	v_add_u32_e32 v144, 0x10800, v5
	v_add_u32_e32 v145, 0x10c00, v5
	v_add_u32_e32 v146, 0x14000, v5
	v_add_u32_e32 v147, 0x14400, v5
	v_add_u32_e32 v148, 0x14800, v5
	v_add_u32_e32 v149, 0x14c00, v5
	v_add_u32_e32 v150, 0x18000, v5
	v_add_u32_e32 v151, 0x18400, v5
	v_add_u32_e32 v152, 0x18800, v5
	v_add_u32_e32 v153, 0x18c00, v5
	v_add_u32_e32 v154, 0x1c000, v5
	v_add_u32_e32 v155, 0x1c400, v5
	v_add_u32_e32 v156, 0x1c800, v5
	v_add_u32_e32 v157, 0x1cc00, v5
	s_ashr_i32 s48, s64, 31
	v_mov_b32_e32 v135, v129
	v_lshl_add_u32 v136, v13, 1, v0
	v_mov_b32_e32 v137, v129
	v_mov_b64_e32 v[138:139], 0x200
	v_mov_b64_e32 v[140:141], 0x1ff
	v_add_u32_e32 v158, s16, v4
	s_movk_i32 s49, 0x1000
	s_barrier
	s_cmp_lt_u32 s94, 4
	s_cbranch_scc1 .Lsp687_skip
	s_setprio 1

.LBB0_687:
	ds_read_b128 v[160:163], v142
	ds_read_b128 v[164:167], v143
	ds_read_b128 v[168:171], v144
	ds_read_b128 v[172:175], v145
	ds_read_b128 v[176:179], v146
	ds_read_b128 v[180:183], v147
	ds_read_b128 v[184:187], v148
	ds_read_b128 v[188:191], v149
	s_add_u32 s26, s24, 0xfff00080
	s_addc_u32 s27, s25, -1
	s_cmp_eq_u32 s54, 60
	s_cselect_b32 s29, s19, s27
	s_cselect_b32 s28, s50, s26
	s_cselect_b32 s27, s17, s53
	s_cselect_b32 s26, s51, s52
	v_lshl_add_u64 v[224:225], s[24:25], 0, v[134:135]
	s_add_i32 m0, s33, 0xc000
	ds_read_b128 v[192:195], v158
	ds_read_b128 v[196:199], v158 offset:1024
	ds_read_b128 v[200:203], v158 offset:2048
	ds_read_b128 v[204:207], v158 offset:3072
	ds_read_b128 v[208:211], v158 offset:4096
	ds_read_b128 v[212:215], v158 offset:5120
	ds_read_b128 v[216:219], v158 offset:6144
	ds_read_b128 v[220:223], v158 offset:7168
	global_load_lds_dwordx4 v[224:225], off
	v_lshl_add_u64 v[224:225], s[24:25], 0, v[136:137]
	s_add_i32 m0, s33, 0xe000
	s_nop 0
	global_load_lds_dwordx4 v[224:225], off
	s_waitcnt vmcnt(8)
	s_waitcnt lgkmcnt(0)
	s_barrier
	s_waitcnt lgkmcnt(0)
	v_mfma_f32_16x16x32_bf16 v[124:127], v[160:163], v[192:195], v[124:127]
	v_mfma_f32_16x16x32_bf16 v[120:123], v[168:171], v[192:195], v[120:123]
	v_mfma_f32_16x16x32_bf16 v[116:119], v[160:163], v[200:203], v[116:119]
	v_mfma_f32_16x16x32_bf16 v[112:115], v[168:171], v[200:203], v[112:115]
	v_mfma_f32_16x16x32_bf16 v[108:111], v[160:163], v[208:211], v[108:111]
	v_mfma_f32_16x16x32_bf16 v[104:107], v[168:171], v[208:211], v[104:107]
	v_mfma_f32_16x16x32_bf16 v[100:103], v[160:163], v[216:219], v[100:103]
	v_mfma_f32_16x16x32_bf16 v[96:99], v[168:171], v[216:219], v[96:99]
	v_mfma_f32_16x16x32_bf16 v[124:127], v[164:167], v[196:199], v[124:127]
	v_mfma_f32_16x16x32_bf16 v[120:123], v[172:175], v[196:199], v[120:123]
	v_mfma_f32_16x16x32_bf16 v[116:119], v[164:167], v[204:207], v[116:119]
	v_mfma_f32_16x16x32_bf16 v[112:115], v[172:175], v[204:207], v[112:115]
	v_mfma_f32_16x16x32_bf16 v[108:111], v[164:167], v[212:215], v[108:111]
	v_mfma_f32_16x16x32_bf16 v[104:107], v[172:175], v[212:215], v[104:107]
	v_mfma_f32_16x16x32_bf16 v[100:103], v[164:167], v[220:223], v[100:103]
	v_mfma_f32_16x16x32_bf16 v[96:99], v[172:175], v[220:223], v[96:99]
	v_mfma_f32_16x16x32_bf16 v[92:95], v[176:179], v[192:195], v[92:95]
	v_mfma_f32_16x16x32_bf16 v[88:91], v[184:187], v[192:195], v[88:91]
	v_mfma_f32_16x16x32_bf16 v[84:87], v[176:179], v[200:203], v[84:87]
	v_mfma_f32_16x16x32_bf16 v[80:83], v[184:187], v[200:203], v[80:83]
	v_mfma_f32_16x16x32_bf16 v[76:79], v[176:179], v[208:211], v[76:79]
	v_mfma_f32_16x16x32_bf16 v[72:75], v[184:187], v[208:211], v[72:75]
	v_mfma_f32_16x16x32_bf16 v[68:71], v[176:179], v[216:219], v[68:71]
	v_mfma_f32_16x16x32_bf16 v[64:67], v[184:187], v[216:219], v[64:67]
	v_mfma_f32_16x16x32_bf16 v[92:95], v[180:183], v[196:199], v[92:95]
	v_mfma_f32_16x16x32_bf16 v[88:91], v[188:191], v[196:199], v[88:91]
	v_mfma_f32_16x16x32_bf16 v[84:87], v[180:183], v[204:207], v[84:87]
	v_mfma_f32_16x16x32_bf16 v[80:83], v[188:191], v[204:207], v[80:83]
	v_mfma_f32_16x16x32_bf16 v[76:79], v[180:183], v[212:215], v[76:79]
	v_mfma_f32_16x16x32_bf16 v[72:75], v[188:191], v[212:215], v[72:75]
	v_mfma_f32_16x16x32_bf16 v[68:71], v[180:183], v[220:223], v[68:71]
	v_mfma_f32_16x16x32_bf16 v[64:67], v[188:191], v[220:223], v[64:67]
	s_barrier
	s_mov_b32 m0, s34
	v_lshl_add_u64 v[224:225], s[26:27], 0, v[128:129]
	s_add_u32 s56, s26, 0x100000
	ds_read_b128 v[192:195], v158 offset:16384
	ds_read_b128 v[196:199], v158 offset:17408
	ds_read_b128 v[200:203], v158 offset:18432
	ds_read_b128 v[204:207], v158 offset:19456
	ds_read_b128 v[208:211], v158 offset:20480
	ds_read_b128 v[212:215], v158 offset:21504
	ds_read_b128 v[216:219], v158 offset:22528
	ds_read_b128 v[220:223], v158 offset:23552
	global_load_lds_dwordx4 v[224:225], off
	v_lshl_add_u64 v[226:227], s[26:27], 0, v[130:131]
	s_mov_b32 m0, s35
	s_addc_u32 s57, s27, 0
	global_load_lds_dwordx4 v[226:227], off
	v_lshl_add_u64 v[228:229], s[56:57], 0, v[128:129]
	s_mov_b32 m0, s36
	v_lshl_add_u64 v[230:231], s[28:29], 0, v[130:131]
	global_load_lds_dwordx4 v[228:229], off
	v_lshl_add_u64 v[228:229], s[56:57], 0, v[130:131]
	s_mov_b32 m0, s37
	s_nop 0
	global_load_lds_dwordx4 v[228:229], off
	v_lshl_add_u64 v[228:229], s[28:29], 0, v[128:129]
	s_mov_b32 m0, s33
	s_nop 0
	global_load_lds_dwordx4 v[228:229], off
	s_mov_b32 m0, s38
	s_nop 0
	global_load_lds_dwordx4 v[230:231], off
	s_waitcnt vmcnt(8)
	s_waitcnt lgkmcnt(0)
	s_barrier
	s_waitcnt lgkmcnt(0)
	v_mfma_f32_16x16x32_bf16 v[60:63], v[160:163], v[192:195], v[60:63]
	v_mfma_f32_16x16x32_bf16 v[56:59], v[168:171], v[192:195], v[56:59]
	v_mfma_f32_16x16x32_bf16 v[52:55], v[160:163], v[200:203], v[52:55]
	v_mfma_f32_16x16x32_bf16 v[48:51], v[168:171], v[200:203], v[48:51]
	v_mfma_f32_16x16x32_bf16 v[44:47], v[160:163], v[208:211], v[44:47]
	v_mfma_f32_16x16x32_bf16 v[40:43], v[168:171], v[208:211], v[40:43]
	v_mfma_f32_16x16x32_bf16 v[36:39], v[160:163], v[216:219], v[36:39]
	v_mfma_f32_16x16x32_bf16 v[32:35], v[168:171], v[216:219], v[32:35]
	v_mfma_f32_16x16x32_bf16 v[60:63], v[164:167], v[196:199], v[60:63]
	v_mfma_f32_16x16x32_bf16 v[56:59], v[172:175], v[196:199], v[56:59]
	v_mfma_f32_16x16x32_bf16 v[52:55], v[164:167], v[204:207], v[52:55]
	v_mfma_f32_16x16x32_bf16 v[48:51], v[172:175], v[204:207], v[48:51]
	v_mfma_f32_16x16x32_bf16 v[44:47], v[164:167], v[212:215], v[44:47]
	v_mfma_f32_16x16x32_bf16 v[40:43], v[172:175], v[212:215], v[40:43]
	v_mfma_f32_16x16x32_bf16 v[36:39], v[164:167], v[220:223], v[36:39]
	v_mfma_f32_16x16x32_bf16 v[32:35], v[172:175], v[220:223], v[32:35]
	v_mfma_f32_16x16x32_bf16 v[28:31], v[176:179], v[192:195], v[28:31]
	v_mfma_f32_16x16x32_bf16 v[24:27], v[184:187], v[192:195], v[24:27]
	v_mfma_f32_16x16x32_bf16 v[20:23], v[176:179], v[200:203], v[20:23]
	v_mfma_f32_16x16x32_bf16 v[16:19], v[184:187], v[200:203], v[16:19]
	v_mfma_f32_16x16x32_bf16 v[12:15], v[176:179], v[208:211], v[12:15]
	v_mfma_f32_16x16x32_bf16 v[8:11], v[184:187], v[208:211], v[8:11]
	v_mfma_f32_16x16x32_bf16 v[4:7], v[176:179], v[216:219], v[4:7]
	v_mfma_f32_16x16x32_bf16 v[0:3], v[184:187], v[216:219], v[0:3]
	v_mfma_f32_16x16x32_bf16 v[28:31], v[180:183], v[196:199], v[28:31]
	v_mfma_f32_16x16x32_bf16 v[24:27], v[188:191], v[196:199], v[24:27]
	v_mfma_f32_16x16x32_bf16 v[20:23], v[180:183], v[204:207], v[20:23]
	v_mfma_f32_16x16x32_bf16 v[16:19], v[188:191], v[204:207], v[16:19]
	v_mfma_f32_16x16x32_bf16 v[12:15], v[180:183], v[212:215], v[12:15]
	v_mfma_f32_16x16x32_bf16 v[8:11], v[188:191], v[212:215], v[8:11]
	v_mfma_f32_16x16x32_bf16 v[4:7], v[180:183], v[220:223], v[4:7]
	v_mfma_f32_16x16x32_bf16 v[0:3], v[188:191], v[220:223], v[0:3]
	s_barrier
	ds_read_b128 v[160:163], v150
	ds_read_b128 v[164:167], v151
	ds_read_b128 v[168:171], v152
	ds_read_b128 v[172:175], v153
	ds_read_b128 v[176:179], v154
	ds_read_b128 v[180:183], v155
	ds_read_b128 v[184:187], v156
	ds_read_b128 v[188:191], v157
	s_add_u32 s28, s28, 0x100000
	s_addc_u32 s29, s29, 0
	s_mov_b32 m0, s39
	v_lshl_add_u64 v[232:233], s[28:29], 0, v[128:129]
	ds_read_b128 v[192:195], v158 offset:32768
	ds_read_b128 v[196:199], v158 offset:33792
	ds_read_b128 v[200:203], v158 offset:34816
	ds_read_b128 v[204:207], v158 offset:35840
	ds_read_b128 v[208:211], v158 offset:36864
	ds_read_b128 v[212:215], v158 offset:37888
	ds_read_b128 v[216:219], v158 offset:38912
	ds_read_b128 v[220:223], v158 offset:39936
	global_load_lds_dwordx4 v[232:233], off
	v_lshl_add_u64 v[232:233], s[28:29], 0, v[130:131]
	s_mov_b32 m0, s40
	s_nop 0
	global_load_lds_dwordx4 v[232:233], off
	s_waitcnt vmcnt(8)
	s_waitcnt lgkmcnt(0)
	s_barrier
	s_waitcnt lgkmcnt(0)
	v_mfma_f32_16x16x32_bf16 v[124:127], v[160:163], v[192:195], v[124:127]
	v_mfma_f32_16x16x32_bf16 v[120:123], v[168:171], v[192:195], v[120:123]
	v_mfma_f32_16x16x32_bf16 v[116:119], v[160:163], v[200:203], v[116:119]
	v_mfma_f32_16x16x32_bf16 v[112:115], v[168:171], v[200:203], v[112:115]
	v_mfma_f32_16x16x32_bf16 v[108:111], v[160:163], v[208:211], v[108:111]
	v_mfma_f32_16x16x32_bf16 v[104:107], v[168:171], v[208:211], v[104:107]
	v_mfma_f32_16x16x32_bf16 v[100:103], v[160:163], v[216:219], v[100:103]
	v_mfma_f32_16x16x32_bf16 v[96:99], v[168:171], v[216:219], v[96:99]
	v_mfma_f32_16x16x32_bf16 v[124:127], v[164:167], v[196:199], v[124:127]
	v_mfma_f32_16x16x32_bf16 v[120:123], v[172:175], v[196:199], v[120:123]
	v_mfma_f32_16x16x32_bf16 v[116:119], v[164:167], v[204:207], v[116:119]
	v_mfma_f32_16x16x32_bf16 v[112:115], v[172:175], v[204:207], v[112:115]
	v_mfma_f32_16x16x32_bf16 v[108:111], v[164:167], v[212:215], v[108:111]
	v_mfma_f32_16x16x32_bf16 v[104:107], v[172:175], v[212:215], v[104:107]
	v_mfma_f32_16x16x32_bf16 v[100:103], v[164:167], v[220:223], v[100:103]
	v_mfma_f32_16x16x32_bf16 v[96:99], v[172:175], v[220:223], v[96:99]
	v_mfma_f32_16x16x32_bf16 v[92:95], v[176:179], v[192:195], v[92:95]
	v_mfma_f32_16x16x32_bf16 v[88:91], v[184:187], v[192:195], v[88:91]
	v_mfma_f32_16x16x32_bf16 v[84:87], v[176:179], v[200:203], v[84:87]
	v_mfma_f32_16x16x32_bf16 v[80:83], v[184:187], v[200:203], v[80:83]
	v_mfma_f32_16x16x32_bf16 v[76:79], v[176:179], v[208:211], v[76:79]
	v_mfma_f32_16x16x32_bf16 v[72:75], v[184:187], v[208:211], v[72:75]
	v_mfma_f32_16x16x32_bf16 v[68:71], v[176:179], v[216:219], v[68:71]
	v_mfma_f32_16x16x32_bf16 v[64:67], v[184:187], v[216:219], v[64:67]
	v_mfma_f32_16x16x32_bf16 v[92:95], v[180:183], v[196:199], v[92:95]
	v_mfma_f32_16x16x32_bf16 v[88:91], v[188:191], v[196:199], v[88:91]
	v_mfma_f32_16x16x32_bf16 v[84:87], v[180:183], v[204:207], v[84:87]
	v_mfma_f32_16x16x32_bf16 v[80:83], v[188:191], v[204:207], v[80:83]
	v_mfma_f32_16x16x32_bf16 v[76:79], v[180:183], v[212:215], v[76:79]
	v_mfma_f32_16x16x32_bf16 v[72:75], v[188:191], v[212:215], v[72:75]
	v_mfma_f32_16x16x32_bf16 v[68:71], v[180:183], v[220:223], v[68:71]
	v_mfma_f32_16x16x32_bf16 v[64:67], v[188:191], v[220:223], v[64:67]
	s_barrier
	s_mov_b32 m0, s42
	v_lshl_add_u64 v[224:225], v[224:225], 0, s[10:11]
	s_add_u32 s26, s26, 0x100080
	ds_read_b128 v[192:195], v158 offset:49152
	ds_read_b128 v[196:199], v158 offset:50176
	ds_read_b128 v[200:203], v158 offset:51200
	ds_read_b128 v[204:207], v158 offset:52224
	ds_read_b128 v[208:211], v158 offset:53248
	ds_read_b128 v[212:215], v158 offset:54272
	ds_read_b128 v[216:219], v158 offset:55296
	ds_read_b128 v[220:223], v158 offset:56320
	global_load_lds_dwordx4 v[224:225], off
	v_lshl_add_u64 v[224:225], v[226:227], 0, s[10:11]
	s_mov_b32 m0, s43
	s_addc_u32 s27, s27, 0
	global_load_lds_dwordx4 v[224:225], off
	v_lshl_add_u64 v[224:225], s[26:27], 0, v[128:129]
	s_mov_b32 m0, s46
	s_nop 0
	global_load_lds_dwordx4 v[224:225], off
	v_lshl_add_u64 v[224:225], s[26:27], 0, v[130:131]
	s_mov_b32 m0, s47
	s_nop 0
	global_load_lds_dwordx4 v[224:225], off
	v_lshl_add_u64 v[224:225], v[228:229], 0, s[10:11]
	s_mov_b32 m0, s44
	s_nop 0
	global_load_lds_dwordx4 v[224:225], off
	v_lshl_add_u64 v[224:225], v[230:231], 0, s[10:11]
	s_mov_b32 m0, s45
	s_nop 0
	global_load_lds_dwordx4 v[224:225], off
	s_waitcnt vmcnt(8)
	s_waitcnt lgkmcnt(0)
	s_barrier
	s_waitcnt lgkmcnt(0)
	v_mfma_f32_16x16x32_bf16 v[60:63], v[160:163], v[192:195], v[60:63]
	v_mfma_f32_16x16x32_bf16 v[56:59], v[168:171], v[192:195], v[56:59]
	v_mfma_f32_16x16x32_bf16 v[52:55], v[160:163], v[200:203], v[52:55]
	v_mfma_f32_16x16x32_bf16 v[48:51], v[168:171], v[200:203], v[48:51]
	v_mfma_f32_16x16x32_bf16 v[44:47], v[160:163], v[208:211], v[44:47]
	v_mfma_f32_16x16x32_bf16 v[40:43], v[168:171], v[208:211], v[40:43]
	v_mfma_f32_16x16x32_bf16 v[36:39], v[160:163], v[216:219], v[36:39]
	v_mfma_f32_16x16x32_bf16 v[32:35], v[168:171], v[216:219], v[32:35]
	v_mfma_f32_16x16x32_bf16 v[60:63], v[164:167], v[196:199], v[60:63]
	v_mfma_f32_16x16x32_bf16 v[56:59], v[172:175], v[196:199], v[56:59]
	v_mfma_f32_16x16x32_bf16 v[52:55], v[164:167], v[204:207], v[52:55]
	v_mfma_f32_16x16x32_bf16 v[48:51], v[172:175], v[204:207], v[48:51]
	v_mfma_f32_16x16x32_bf16 v[44:47], v[164:167], v[212:215], v[44:47]
	v_mfma_f32_16x16x32_bf16 v[40:43], v[172:175], v[212:215], v[40:43]
	v_mfma_f32_16x16x32_bf16 v[36:39], v[164:167], v[220:223], v[36:39]
	v_mfma_f32_16x16x32_bf16 v[32:35], v[172:175], v[220:223], v[32:35]
	v_mfma_f32_16x16x32_bf16 v[28:31], v[176:179], v[192:195], v[28:31]
	v_mfma_f32_16x16x32_bf16 v[24:27], v[184:187], v[192:195], v[24:27]
	v_mfma_f32_16x16x32_bf16 v[20:23], v[176:179], v[200:203], v[20:23]
	v_mfma_f32_16x16x32_bf16 v[16:19], v[184:187], v[200:203], v[16:19]
	v_mfma_f32_16x16x32_bf16 v[12:15], v[176:179], v[208:211], v[12:15]
	v_mfma_f32_16x16x32_bf16 v[8:11], v[184:187], v[208:211], v[8:11]
	v_mfma_f32_16x16x32_bf16 v[4:7], v[176:179], v[216:219], v[4:7]
	v_mfma_f32_16x16x32_bf16 v[0:3], v[184:187], v[216:219], v[0:3]
	v_mfma_f32_16x16x32_bf16 v[28:31], v[180:183], v[196:199], v[28:31]
	v_mfma_f32_16x16x32_bf16 v[24:27], v[188:191], v[196:199], v[24:27]
	v_mfma_f32_16x16x32_bf16 v[20:23], v[180:183], v[204:207], v[20:23]
	v_mfma_f32_16x16x32_bf16 v[16:19], v[188:191], v[204:207], v[16:19]
	v_mfma_f32_16x16x32_bf16 v[12:15], v[180:183], v[212:215], v[12:15]
	v_mfma_f32_16x16x32_bf16 v[8:11], v[188:191], v[212:215], v[8:11]
	v_mfma_f32_16x16x32_bf16 v[4:7], v[180:183], v[220:223], v[4:7]
	v_mfma_f32_16x16x32_bf16 v[0:3], v[188:191], v[220:223], v[0:3]
	s_barrier
	s_add_i32 s54, s54, 2
	s_add_u32 s24, s24, 0x100
	s_addc_u32 s25, s25, 0
	s_add_u32 s52, s52, 0x100
	s_addc_u32 s53, s53, 0
	s_cmp_gt_u32 s54, 61
	s_cbranch_scc0 .LBB0_687
	s_and_b64 vcc, exec, s[12:13]
	s_cbranch_vccz .LBB0_690
	s_barrier

.LBB0_930:
	v_readlane_b32 s10, v254, 0
	v_readlane_b32 s11, v254, 1
	s_load_dwordx2 s[10:11], s[10:11], 0xa0
	s_mov_b64 s[12:13], 0x80
	v_lshl_add_u64 v[6:7], v[6:7], 0, s[12:13]
	s_waitcnt vmcnt(2)
	s_barrier
	s_waitcnt lgkmcnt(0)
	s_add_u32 s10, s10, 0x55400000
	s_addc_u32 s11, s11, 0
	s_add_i32 s51, s33, 0x18000
	s_lshl_b32 s5, s94, 12
	s_mov_b32 m0, s51
	s_add_i32 s52, s33, 0x1a000
	s_lshl_b32 s16, s4, 13
	s_and_b32 s5, s5, 0x3000
	global_load_lds_dwordx4 v[6:7], off
	v_lshl_add_u64 v[4:5], v[4:5], 0, s[12:13]
	s_mov_b32 m0, s52
	s_add_i32 s53, s33, 0x8000
	s_add_i32 s54, s33, 0xa000
	global_load_lds_dwordx4 v[4:5], off
	v_lshl_add_u64 v[0:1], v[0:1], 0, s[12:13]
	s_mov_b32 m0, s53
	s_add_u32 s14, s40, 0x80080
	global_load_lds_dwordx4 v[0:1], off
	v_lshl_add_u64 v[0:1], v[2:3], 0, s[12:13]
	s_mov_b32 m0, s54
	s_addc_u32 s15, s41, 0
	s_add_i32 s55, s33, 0x1c000
	global_load_lds_dwordx4 v[0:1], off
	v_lshl_add_u64 v[0:1], s[14:15], 0, v[162:163]
	s_mov_b32 m0, s55
	s_add_i32 s56, s33, 0x1e000
	global_load_lds_dwordx4 v[0:1], off
	v_lshl_add_u64 v[0:1], s[14:15], 0, v[166:167]
	s_mov_b32 m0, s56
	v_lshlrev_b32_e32 v4, 2, v14
	global_load_lds_dwordx4 v[0:1], off
	v_lshrrev_b32_e32 v0, 1, v14
	v_and_b32_e32 v1, 15, v14
	v_and_b32_e32 v0, 24, v0
	v_lshlrev_b32_e32 v2, 1, v0
	v_lshlrev_b32_e32 v3, 6, v1
	v_and_b32_e32 v4, 32, v4
	s_add_i32 s5, s5, 0
	v_bitop3_b32 v2, v3, v4, v2 bitop3:0x36
	s_cmpk_lt_u32 s65, 0x100
	v_lshl_or_b32 v188, s4, 6, v1
	v_add_u32_e32 v3, s5, v2
	s_cselect_b64 s[14:15], -1, 0
	s_lshl_b64 s[4:5], s[94:95], 9
	s_ashr_i32 s57, s64, 31
	s_ashr_i32 s58, s68, 31
	v_readlane_b32 s18, v254, 14
	v_readlane_b32 s19, v254, 15
	s_add_u32 s4, s18, s4
	v_lshlrev_b32_e32 v168, 5, v1
	s_addc_u32 s5, s19, s5
	v_add_u32_e32 v4, 0, v2
	v_mov_b32_e32 v1, v169
	v_add_u32_e32 v189, 0x10000, v3
	v_add_u32_e32 v190, 0x10400, v3
	v_add_u32_e32 v191, 0x10800, v3
	v_add_u32_e32 v192, 0x10c00, v3
	v_add_u32_e32 v193, 0x14000, v3
	v_add_u32_e32 v194, 0x14400, v3
	v_add_u32_e32 v195, 0x14800, v3
	v_add_u32_e32 v196, 0x14c00, v3
	v_add_u32_e32 v197, 0x18000, v3
	v_add_u32_e32 v198, 0x18400, v3
	v_add_u32_e32 v199, 0x18800, v3
	v_add_u32_e32 v200, 0x18c00, v3
	v_add_u32_e32 v201, 0x1c000, v3
	v_add_u32_e32 v202, 0x1c400, v3
	v_add_u32_e32 v203, 0x1c800, v3
	v_add_u32_e32 v204, 0x1cc00, v3
	v_lshl_add_u64 v[2:3], s[4:5], 0, v[168:169]
	v_lshl_add_u64 v[170:171], v[2:3], 0, v[0:1]
	v_lshlrev_b32_e32 v0, 15, v8
	v_and_b32_e32 v0, 0xffff0000, v0
	v_lshl_add_u32 v0, v9, 12, v0
	v_and_b32_e32 v1, 1, v8
	v_lshl_or_b32 v0, v1, 6, v0
	v_lshl_add_u32 v172, v10, 1, v0
	v_lshlrev_b32_e32 v0, 15, v11
	v_and_b32_e32 v0, 0xffff0000, v0
	s_waitcnt vmcnt(6)
	v_lshl_add_u32 v0, v12, 12, v0
	v_and_b32_e32 v1, 1, v11
	v_lshl_or_b32 v0, v1, 6, v0
	v_mov_b32_e32 v173, v169
	v_lshl_add_u32 v174, v13, 1, v0
	v_mov_b32_e32 v175, v169
	v_mov_b64_e32 v[176:177], 0x1000
	v_mov_b64_e32 v[178:179], 0xfff
	v_add_u32_e32 v205, s16, v4
	s_mov_b32 s59, 0xffffff
	s_mov_b64 s[16:17], 0x10000
	s_mov_b64 s[18:19], 0x12000
	s_mov_b64 s[20:21], 0x14000
	s_mov_b64 s[22:23], 0x16000
	v_mov_b32_e32 v206, 2
	s_barrier
	s_mov_b32 s74, -1
	s_cmp_lt_u32 s94, 4
	s_cbranch_scc1 .Lsp940_skip
	s_setprio 1

.LBB0_940:
	s_add_u32 s72, s38, 0xfff80000
	s_addc_u32 s73, s39, -1
	s_mov_b32 m0, s53
	s_nop 0
	global_load_lds_dwordx4 v160, s[72:73]
	s_mov_b32 m0, s54
	s_nop 0
	global_load_lds_dwordx4 v164, s[72:73]
	ds_read_b128 v[16:19], v189
	ds_read_b128 v[20:23], v190
	ds_read_b128 v[24:27], v191
	ds_read_b128 v[28:31], v192
	ds_read_b128 v[0:3], v193
	ds_read_b128 v[4:7], v194
	ds_read_b128 v[8:11], v195
	ds_read_b128 v[12:15], v196
	s_add_u32 s40, s38, 0xfff80080
	s_addc_u32 s41, s39, -1
	s_cmp_eq_u32 s64, 28
	s_cselect_b32 s43, s27, s41
	s_cselect_b32 s42, s35, s40
	s_cselect_b32 s41, s25, s61
	s_cselect_b32 s40, s37, s60
	s_add_i32 m0, s33, 0xc000
	ds_read_b128 v[180:183], v205
	ds_read_b128 v[184:187], v205 offset:1024
	ds_read_b128 v[208:211], v205 offset:2048
	ds_read_b128 v[212:215], v205 offset:3072
	ds_read_b128 v[216:219], v205 offset:4096
	ds_read_b128 v[220:223], v205 offset:5120
	ds_read_b128 v[224:227], v205 offset:6144
	ds_read_b128 v[228:231], v205 offset:7168
	global_load_lds_dwordx4 v172, s[38:39]
	s_add_i32 m0, s33, 0xe000
	s_nop 0
	global_load_lds_dwordx4 v174, s[38:39]
	s_waitcnt vmcnt(8)
	s_waitcnt lgkmcnt(0)
	s_barrier
	s_waitcnt lgkmcnt(0)
	s_bitcmp1_b32 s74, 0
	s_cbranch_scc0 .Lp8s_0
	v_mfma_f32_16x16x128_f8f6f4 v[156:159], v[16:23], v[180:187], v[156:159]

.Lp8s_7:
	s_bitcmp1_b32 s74, 2
	s_cbranch_scc0 .Lp8s_8
	v_mfma_f32_16x16x128_f8f6f4 v[148:151], v[0:7], v[180:187], v[148:151]

.Lp8s_15:
	s_barrier
	s_mov_b32 m0, s44
	v_lshl_add_u64 v[180:181], s[40:41], 0, v[162:163]
	s_add_u32 s62, s40, 0x80000
	ds_read_b128 v[208:211], v205 offset:16384
	ds_read_b128 v[212:215], v205 offset:17408
	ds_read_b128 v[216:219], v205 offset:18432
	ds_read_b128 v[220:223], v205 offset:19456
	ds_read_b128 v[224:227], v205 offset:20480
	ds_read_b128 v[228:231], v205 offset:21504
	ds_read_b128 v[232:235], v205 offset:22528
	ds_read_b128 v[236:239], v205 offset:23552
	global_load_lds_dwordx4 v[180:181], off
	v_lshl_add_u64 v[182:183], s[40:41], 0, v[166:167]
	s_mov_b32 m0, s45
	s_addc_u32 s63, s41, 0
	global_load_lds_dwordx4 v[182:183], off
	s_mov_b32 m0, s46
	s_nop 0
	global_load_lds_dwordx4 v162, s[62:63]
	s_mov_b32 m0, s47
	s_nop 0
	global_load_lds_dwordx4 v166, s[62:63]
	s_waitcnt vmcnt(6)
	s_waitcnt lgkmcnt(0)
	s_barrier
	s_waitcnt lgkmcnt(0)
	s_bitcmp1_b32 s74, 16
	s_cbranch_scc0 .Lp8s_16
	v_mfma_f32_16x16x128_f8f6f4 v[92:95], v[16:23], v[208:215], v[92:95]

.Lp8s_23:
	s_bitcmp1_b32 s74, 18
	s_cbranch_scc0 .Lp8s_24
	v_mfma_f32_16x16x128_f8f6f4 v[84:87], v[0:7], v[208:215], v[84:87]

.Lp8s_31:
	s_barrier
	s_mov_b32 m0, s33
	s_nop 0
	global_load_lds_dwordx4 v160, s[42:43]
	s_mov_b32 m0, s48
	s_nop 0
	global_load_lds_dwordx4 v164, s[42:43]
	ds_read_b128 v[0:3], v197
	ds_read_b128 v[4:7], v198
	ds_read_b128 v[8:11], v199
	ds_read_b128 v[12:15], v200
	ds_read_b128 v[16:19], v201
	ds_read_b128 v[20:23], v202
	ds_read_b128 v[24:27], v203
	ds_read_b128 v[28:31], v204
	s_add_u32 s42, s42, 0x80000
	s_addc_u32 s43, s43, 0
	s_mov_b32 m0, s49
	ds_read_b128 v[208:211], v205 offset:32768
	ds_read_b128 v[212:215], v205 offset:33792
	ds_read_b128 v[216:219], v205 offset:34816
	ds_read_b128 v[220:223], v205 offset:35840
	ds_read_b128 v[224:227], v205 offset:36864
	ds_read_b128 v[228:231], v205 offset:37888
	ds_read_b128 v[232:235], v205 offset:38912
	ds_read_b128 v[236:239], v205 offset:39936
	global_load_lds_dwordx4 v160, s[42:43]
	s_mov_b32 m0, s50
	s_nop 0
	global_load_lds_dwordx4 v164, s[42:43]
	s_waitcnt vmcnt(8)
	s_waitcnt lgkmcnt(0)
	s_barrier
	s_waitcnt lgkmcnt(0)
	s_bitcmp1_b32 s74, 0
	s_cbranch_scc0 .Lp8s_32
	v_mfma_f32_16x16x128_f8f6f4 v[156:159], v[0:7], v[208:215], v[156:159]

.Lp8s_39:
	s_bitcmp1_b32 s74, 2
	s_cbranch_scc0 .Lp8s_40
	v_mfma_f32_16x16x128_f8f6f4 v[148:151], v[16:23], v[208:215], v[148:151]

.Lp8s_47:
	s_barrier
	s_mov_b32 m0, s51
	v_lshl_add_u64 v[180:181], v[180:181], 0, s[12:13]
	s_add_u32 s40, s40, 0x80080
	ds_read_b128 v[208:211], v205 offset:49152
	ds_read_b128 v[212:215], v205 offset:50176
	ds_read_b128 v[216:219], v205 offset:51200
	ds_read_b128 v[220:223], v205 offset:52224
	ds_read_b128 v[224:227], v205 offset:53248
	ds_read_b128 v[228:231], v205 offset:54272
	ds_read_b128 v[232:235], v205 offset:55296
	ds_read_b128 v[236:239], v205 offset:56320
	global_load_lds_dwordx4 v[180:181], off
	v_lshl_add_u64 v[180:181], v[182:183], 0, s[12:13]
	s_mov_b32 m0, s52
	s_addc_u32 s41, s41, 0
	global_load_lds_dwordx4 v[180:181], off
	s_mov_b32 m0, s55
	s_nop 0
	global_load_lds_dwordx4 v162, s[40:41]
	s_mov_b32 m0, s56
	s_nop 0
	global_load_lds_dwordx4 v166, s[40:41]
	s_waitcnt vmcnt(6)
	s_waitcnt lgkmcnt(0)
	s_barrier
	s_waitcnt lgkmcnt(0)
	s_bitcmp1_b32 s74, 16
	s_cbranch_scc0 .Lp8s_48
	v_mfma_f32_16x16x128_f8f6f4 v[92:95], v[0:7], v[208:215], v[92:95]

.Lp8s_55:
	s_bitcmp1_b32 s74, 18
	s_cbranch_scc0 .Lp8s_56
	v_mfma_f32_16x16x128_f8f6f4 v[84:87], v[16:23], v[208:215], v[84:87]

.Lp8s_63:
	s_barrier
	s_add_i32 s64, s64, 2
	s_add_u32 s38, s38, 0x100
	s_addc_u32 s39, s39, 0
	s_add_u32 s60, s60, 0x100
	s_addc_u32 s61, s61, 0
	s_cmp_gt_u32 s64, 29
	s_cbranch_scc0 .LBB0_940
	s_nop 15
	s_nop 15
	s_and_b64 vcc, exec, s[14:15]
	s_cbranch_vccz .LBB0_943
	s_barrier

.LBB0_1348:
	v_readlane_b32 s10, v254, 21
	v_readlane_b32 s11, v254, 22
	s_add_u32 s8, s10, 0x4d400000
	s_addc_u32 s9, s11, 0
	s_add_u32 s45, s10, 0x24000
	s_addc_u32 s46, s11, 0
	s_lshl_b32 s1, s94, 5
	s_and_b32 s1, s1, 0x60
	s_lshl_b32 s14, s0, 13
	s_lshl_b32 s13, s1, 7
	s_add_i32 s47, s25, 0x18000
	s_mov_b64 s[10:11], 0x80
	s_add_i32 s48, s25, 0x1a000
	v_lshl_add_u64 v[2:3], v[2:3], 0, s[10:11]
	s_mov_b32 m0, s47
	s_add_u32 s16, s26, 0x1000
	s_waitcnt vmcnt(2)
	s_barrier
	global_load_lds_dwordx4 v[2:3], off
	v_lshl_add_u64 v[0:1], v[0:1], 0, s[10:11]
	s_mov_b32 m0, s48
	s_addc_u32 s17, s27, 0
	s_add_i32 s49, s25, 0x8000
	global_load_lds_dwordx4 v[0:1], off
	v_lshl_add_u64 v[0:1], s[16:17], 0, v[160:161]
	s_mov_b32 m0, s49
	s_add_i32 s50, s25, 0xa000
	global_load_lds_dwordx4 v[0:1], off
	v_lshl_add_u64 v[0:1], s[16:17], 0, v[164:165]
	s_add_u32 s16, s28, 0x200080
	s_mov_b32 m0, s50
	s_addc_u32 s17, s29, 0
	s_add_i32 s51, s25, 0x1c000
	global_load_lds_dwordx4 v[0:1], off
	v_lshl_add_u64 v[0:1], s[16:17], 0, v[162:163]
	s_mov_b32 m0, s51
	s_add_i32 s52, s25, 0x1e000
	global_load_lds_dwordx4 v[0:1], off
	v_lshl_add_u64 v[0:1], s[16:17], 0, v[166:167]
	s_mov_b32 m0, s52
	v_lshlrev_b32_e32 v3, 2, v6
	global_load_lds_dwordx4 v[0:1], off
	v_and_b32_e32 v0, 15, v6
	v_bfe_u32 v1, v6, 4, 2
	v_lshl_or_b32 v206, s0, 6, v0
	v_lshlrev_b32_e32 v2, 4, v1
	v_lshlrev_b32_e32 v0, 6, v0
	v_and_b32_e32 v3, 32, v3
	v_bitop3_b32 v0, v0, v3, v2 bitop3:0x36
	s_add_i32 s13, s13, 0
	v_add_u32_e32 v2, s13, v0
	v_add_u32_e32 v3, 0, v0
	v_add_u32_e32 v0, v4, v7
	v_lshl_or_b32 v223, v1, 2, s1
	v_add3_u32 v0, v0, v5, v8
	v_mov_b32_e32 v1, v163
	s_mov_b64 s[0:1], 0x9000
	s_waitcnt vmcnt(6)
	v_lshl_add_u64 v[168:169], v[0:1], 0, s[0:1]
	v_add_u32_e32 v0, v9, v11
	s_cmpk_lt_u32 s65, 0x100
	v_add3_u32 v0, v0, v10, v12
	s_sext_i32_i8 s54, s12
	s_cselect_b64 s[12:13], -1, 0
	v_add_u32_e32 v207, 0x10000, v2
	v_add_u32_e32 v208, 0x10400, v2
	v_add_u32_e32 v209, 0x10800, v2
	v_add_u32_e32 v210, 0x10c00, v2
	v_add_u32_e32 v211, 0x14000, v2
	v_add_u32_e32 v212, 0x14400, v2
	v_add_u32_e32 v213, 0x14800, v2
	v_add_u32_e32 v214, 0x14c00, v2
	v_add_u32_e32 v215, 0x18000, v2
	v_add_u32_e32 v216, 0x18400, v2
	v_add_u32_e32 v217, 0x18800, v2
	v_add_u32_e32 v218, 0x18c00, v2
	v_add_u32_e32 v219, 0x1c000, v2
	v_add_u32_e32 v220, 0x1c400, v2
	v_add_u32_e32 v221, 0x1c800, v2
	v_add_u32_e32 v222, 0x1cc00, v2
	s_ashr_i32 s53, s64, 31
	v_lshl_add_u64 v[170:171], v[0:1], 0, s[0:1]
	v_mov_b64_e32 v[172:173], 0x400
	v_mov_b64_e32 v[174:175], 0x3ff
	v_add_u32_e32 v224, s14, v3
	s_mov_b32 s14, 0x3d800000
	s_barrier
	s_cmp_lt_u32 s94, 4
	s_cbranch_scc1 .Lsp1358_skip
	s_setprio 1

.LBB0_1358:
	s_add_u32 s30, s26, 0x1000
	s_addc_u32 s31, s27, 0
	s_mov_b32 m0, s49
	s_nop 0
	global_load_lds_dwordx4 v160, s[30:31]
	s_mov_b32 m0, s50
	s_nop 0
	global_load_lds_dwordx4 v164, s[30:31]
	ds_read_b128 v[16:19], v207
	ds_read_b128 v[20:23], v208
	ds_read_b128 v[24:27], v209
	ds_read_b128 v[28:31], v210
	ds_read_b128 v[0:3], v211
	ds_read_b128 v[4:7], v212
	ds_read_b128 v[8:11], v213
	ds_read_b128 v[12:15], v214
	s_add_u32 s28, s26, 0x10000
	s_addc_u32 s29, s27, 0
	s_cmpk_eq_i32 s59, 0x7c
	s_cselect_b32 s36, s55, s28
	s_cselect_b32 s37, s19, s29
	s_cselect_b32 s34, s56, s57
	s_cselect_b32 s35, s17, s58
	s_add_i32 m0, s25, 0xc000
	ds_read_b128 v[176:179], v224
	ds_read_b128 v[180:183], v224 offset:1024
	ds_read_b128 v[184:187], v224 offset:2048
	ds_read_b128 v[188:191], v224 offset:3072
	ds_read_b128 v[192:195], v224 offset:4096
	ds_read_b128 v[196:199], v224 offset:5120
	ds_read_b128 v[226:229], v224 offset:6144
	ds_read_b128 v[230:233], v224 offset:7168
	global_load_lds_dwordx4 v168, s[26:27]
	s_add_i32 m0, s25, 0xe000
	s_nop 0
	global_load_lds_dwordx4 v170, s[26:27]
	s_waitcnt vmcnt(8)
	s_waitcnt lgkmcnt(0)
	s_barrier
	s_waitcnt lgkmcnt(0)
	v_mfma_f32_16x16x128_f8f6f4 v[156:159], v[16:23], v[176:183], v[156:159]
	v_mfma_f32_16x16x128_f8f6f4 v[152:155], v[24:31], v[176:183], v[152:155]
	v_mfma_f32_16x16x128_f8f6f4 v[144:147], v[16:23], v[184:191], v[144:147]
	v_mfma_f32_16x16x128_f8f6f4 v[136:139], v[24:31], v[184:191], v[136:139]
	v_mfma_f32_16x16x128_f8f6f4 v[124:127], v[16:23], v[192:199], v[124:127]
	v_mfma_f32_16x16x128_f8f6f4 v[120:123], v[24:31], v[192:199], v[120:123]
	v_mfma_f32_16x16x128_f8f6f4 v[112:115], v[16:23], v[226:233], v[112:115]
	v_mfma_f32_16x16x128_f8f6f4 v[104:107], v[24:31], v[226:233], v[104:107]
	v_mfma_f32_16x16x128_f8f6f4 v[148:151], v[0:7], v[176:183], v[148:151]
	v_mfma_f32_16x16x128_f8f6f4 v[140:143], v[8:15], v[176:183], v[140:143]
	v_mfma_f32_16x16x128_f8f6f4 v[132:135], v[0:7], v[184:191], v[132:135]
	v_mfma_f32_16x16x128_f8f6f4 v[128:131], v[8:15], v[184:191], v[128:131]
	v_mfma_f32_16x16x128_f8f6f4 v[116:119], v[0:7], v[192:199], v[116:119]
	v_mfma_f32_16x16x128_f8f6f4 v[108:111], v[8:15], v[192:199], v[108:111]
	v_mfma_f32_16x16x128_f8f6f4 v[100:103], v[0:7], v[226:233], v[100:103]
	v_mfma_f32_16x16x128_f8f6f4 v[96:99], v[8:15], v[226:233], v[96:99]
	s_barrier
	s_mov_b32 m0, s33
	v_lshl_add_u64 v[176:177], s[34:35], 0, v[162:163]
	s_add_u32 s26, s34, 0x200000
	ds_read_b128 v[180:183], v224 offset:16384
	ds_read_b128 v[184:187], v224 offset:17408
	ds_read_b128 v[188:191], v224 offset:18432
	ds_read_b128 v[192:195], v224 offset:19456
	ds_read_b128 v[196:199], v224 offset:20480
	ds_read_b128 v[200:203], v224 offset:21504
	ds_read_b128 v[226:229], v224 offset:22528
	ds_read_b128 v[230:233], v224 offset:23552
	global_load_lds_dwordx4 v[176:177], off
	v_lshl_add_u64 v[178:179], s[34:35], 0, v[166:167]
	s_mov_b32 m0, s38
	s_addc_u32 s27, s35, 0
	global_load_lds_dwordx4 v[178:179], off
	s_mov_b32 m0, s39
	s_nop 0
	global_load_lds_dwordx4 v162, s[26:27]
	s_mov_b32 m0, s40
	s_nop 0
	global_load_lds_dwordx4 v166, s[26:27]
	s_waitcnt vmcnt(6)
	s_waitcnt lgkmcnt(0)
	s_barrier
	s_waitcnt lgkmcnt(0)
	v_mfma_f32_16x16x128_f8f6f4 v[92:95], v[16:23], v[180:187], v[92:95]
	v_mfma_f32_16x16x128_f8f6f4 v[88:91], v[24:31], v[180:187], v[88:91]
	v_mfma_f32_16x16x128_f8f6f4 v[80:83], v[16:23], v[188:195], v[80:83]
	v_mfma_f32_16x16x128_f8f6f4 v[72:75], v[24:31], v[188:195], v[72:75]
	v_mfma_f32_16x16x128_f8f6f4 v[64:67], v[16:23], v[196:203], v[64:67]
	v_mfma_f32_16x16x128_f8f6f4 v[56:59], v[24:31], v[196:203], v[56:59]
	v_mfma_f32_16x16x128_f8f6f4 v[48:51], v[16:23], v[226:233], v[48:51]
	v_mfma_f32_16x16x128_f8f6f4 v[40:43], v[24:31], v[226:233], v[40:43]
	v_mfma_f32_16x16x128_f8f6f4 v[84:87], v[0:7], v[180:187], v[84:87]
	v_mfma_f32_16x16x128_f8f6f4 v[76:79], v[8:15], v[180:187], v[76:79]
	v_mfma_f32_16x16x128_f8f6f4 v[68:71], v[0:7], v[188:195], v[68:71]
	v_mfma_f32_16x16x128_f8f6f4 v[60:63], v[8:15], v[188:195], v[60:63]
	v_mfma_f32_16x16x128_f8f6f4 v[52:55], v[0:7], v[196:203], v[52:55]
	v_mfma_f32_16x16x128_f8f6f4 v[44:47], v[8:15], v[196:203], v[44:47]
	v_mfma_f32_16x16x128_f8f6f4 v[36:39], v[0:7], v[226:233], v[36:39]
	v_mfma_f32_16x16x128_f8f6f4 v[32:35], v[8:15], v[226:233], v[32:35]
	s_barrier
	s_mov_b32 m0, s25
	s_nop 0
	global_load_lds_dwordx4 v160, s[36:37]
	s_mov_b32 m0, s41
	s_nop 0
	global_load_lds_dwordx4 v164, s[36:37]
	ds_read_b128 v[0:3], v215
	ds_read_b128 v[4:7], v216
	ds_read_b128 v[8:11], v217
	ds_read_b128 v[12:15], v218
	ds_read_b128 v[16:19], v219
	ds_read_b128 v[20:23], v220
	ds_read_b128 v[24:27], v221
	ds_read_b128 v[28:31], v222
	s_add_u32 s26, s36, 0x8000
	s_addc_u32 s27, s37, 0
	s_mov_b32 m0, s42
	ds_read_b128 v[180:183], v224 offset:32768
	ds_read_b128 v[184:187], v224 offset:33792
	ds_read_b128 v[188:191], v224 offset:34816
	ds_read_b128 v[192:195], v224 offset:35840
	ds_read_b128 v[196:199], v224 offset:36864
	ds_read_b128 v[200:203], v224 offset:37888
	ds_read_b128 v[226:229], v224 offset:38912
	ds_read_b128 v[230:233], v224 offset:39936
	global_load_lds_dwordx4 v160, s[26:27]
	s_mov_b32 m0, s43
	s_nop 0
	global_load_lds_dwordx4 v164, s[26:27]
	s_waitcnt vmcnt(8)
	s_waitcnt lgkmcnt(0)
	s_barrier
	s_waitcnt lgkmcnt(0)
	v_mfma_f32_16x16x128_f8f6f4 v[156:159], v[0:7], v[180:187], v[156:159]
	v_mfma_f32_16x16x128_f8f6f4 v[152:155], v[8:15], v[180:187], v[152:155]
	v_mfma_f32_16x16x128_f8f6f4 v[144:147], v[0:7], v[188:195], v[144:147]
	v_mfma_f32_16x16x128_f8f6f4 v[136:139], v[8:15], v[188:195], v[136:139]
	v_mfma_f32_16x16x128_f8f6f4 v[124:127], v[0:7], v[196:203], v[124:127]
	v_mfma_f32_16x16x128_f8f6f4 v[120:123], v[8:15], v[196:203], v[120:123]
	v_mfma_f32_16x16x128_f8f6f4 v[112:115], v[0:7], v[226:233], v[112:115]
	v_mfma_f32_16x16x128_f8f6f4 v[104:107], v[8:15], v[226:233], v[104:107]
	v_mfma_f32_16x16x128_f8f6f4 v[148:151], v[16:23], v[180:187], v[148:151]
	v_mfma_f32_16x16x128_f8f6f4 v[140:143], v[24:31], v[180:187], v[140:143]
	v_mfma_f32_16x16x128_f8f6f4 v[132:135], v[16:23], v[188:195], v[132:135]
	v_mfma_f32_16x16x128_f8f6f4 v[128:131], v[24:31], v[188:195], v[128:131]
	v_mfma_f32_16x16x128_f8f6f4 v[116:119], v[16:23], v[196:203], v[116:119]
	v_mfma_f32_16x16x128_f8f6f4 v[108:111], v[24:31], v[196:203], v[108:111]
	v_mfma_f32_16x16x128_f8f6f4 v[100:103], v[16:23], v[226:233], v[100:103]
	v_mfma_f32_16x16x128_f8f6f4 v[96:99], v[24:31], v[226:233], v[96:99]
	s_barrier
	s_mov_b32 m0, s47
	v_lshl_add_u64 v[176:177], v[176:177], 0, s[10:11]
	s_add_u32 s26, s34, 0x200080
	ds_read_b128 v[180:183], v224 offset:49152
	ds_read_b128 v[184:187], v224 offset:50176
	ds_read_b128 v[188:191], v224 offset:51200
	ds_read_b128 v[192:195], v224 offset:52224
	ds_read_b128 v[196:199], v224 offset:53248
	ds_read_b128 v[200:203], v224 offset:54272
	ds_read_b128 v[226:229], v224 offset:55296
	ds_read_b128 v[230:233], v224 offset:56320
	global_load_lds_dwordx4 v[176:177], off
	v_lshl_add_u64 v[176:177], v[178:179], 0, s[10:11]
	s_mov_b32 m0, s48
	s_addc_u32 s27, s35, 0
	global_load_lds_dwordx4 v[176:177], off
	s_mov_b32 m0, s51
	s_nop 0
	global_load_lds_dwordx4 v162, s[26:27]
	s_mov_b32 m0, s52
	s_nop 0
	global_load_lds_dwordx4 v166, s[26:27]
	s_waitcnt vmcnt(6)
	s_waitcnt lgkmcnt(0)
	s_barrier
	s_waitcnt lgkmcnt(0)
	v_mfma_f32_16x16x128_f8f6f4 v[92:95], v[0:7], v[180:187], v[92:95]
	v_mfma_f32_16x16x128_f8f6f4 v[88:91], v[8:15], v[180:187], v[88:91]
	v_mfma_f32_16x16x128_f8f6f4 v[80:83], v[0:7], v[188:195], v[80:83]
	v_mfma_f32_16x16x128_f8f6f4 v[72:75], v[8:15], v[188:195], v[72:75]
	v_mfma_f32_16x16x128_f8f6f4 v[64:67], v[0:7], v[196:203], v[64:67]
	v_mfma_f32_16x16x128_f8f6f4 v[56:59], v[8:15], v[196:203], v[56:59]
	v_mfma_f32_16x16x128_f8f6f4 v[48:51], v[0:7], v[226:233], v[48:51]
	v_mfma_f32_16x16x128_f8f6f4 v[40:43], v[8:15], v[226:233], v[40:43]
	v_mfma_f32_16x16x128_f8f6f4 v[84:87], v[16:23], v[180:187], v[84:87]
	v_mfma_f32_16x16x128_f8f6f4 v[76:79], v[24:31], v[180:187], v[76:79]
	v_mfma_f32_16x16x128_f8f6f4 v[68:71], v[16:23], v[188:195], v[68:71]
	v_mfma_f32_16x16x128_f8f6f4 v[60:63], v[24:31], v[188:195], v[60:63]
	v_mfma_f32_16x16x128_f8f6f4 v[52:55], v[16:23], v[196:203], v[52:55]
	v_mfma_f32_16x16x128_f8f6f4 v[44:47], v[24:31], v[196:203], v[44:47]
	v_mfma_f32_16x16x128_f8f6f4 v[36:39], v[16:23], v[226:233], v[36:39]
	v_mfma_f32_16x16x128_f8f6f4 v[32:35], v[24:31], v[226:233], v[32:35]
	s_barrier
	s_add_i32 s59, s59, 2
	s_add_u32 s57, s57, 0x100
	s_addc_u32 s58, s58, 0
	s_cmpk_gt_u32 s59, 0x7d
	s_mov_b64 s[26:27], s[28:29]
	s_cbranch_scc0 .LBB0_1358
	s_nop 15
	s_nop 15
	s_and_b64 vcc, exec, s[12:13]
	s_cbranch_vccz .LBB0_1361
	s_barrier
